# attention tile loop without wave-uniform branches inside the segments: tiles past the end re-fetch the last tile (staged to the dump area), QK always runs, one unconditional counted wait
# speedup vs baseline: 1.0009x; 1.0009x over previous
; #define LAS __attribute__((address_space(3)))
; __device__ __forceinline__ void lds_barrier() { asm volatile("s_waitcnt lgkmcnt(0)" ::: "memory"); __builtin_amdgcn_s_barrier(); asm volatile("" ::: "memory"); }
; #define AT_LOADK(t) do { const int kr_ = AT_KROW(t); _Pragma("unroll") for (int i_ = 0; i_ < 2; ++i_) kreg[i_] = *(const u32x4*)(Kp + (size_t)(kr_ + prow0 + 32 * i_) * 512 + pch * 8); } while (0)
; #define AT_LOADV(t) do { const int kr_ = AT_KROW(t); _Pragma("unroll") for (int i_ = 0; i_ < 2; ++i_) vreg[i_] = *(const u32x4*)(Vp + (size_t)(kr_ + prow0 + 32 * i_) * 512 + pch * 8); } while (0)
; #define AT_STOREK(st) do { _Pragma("unroll") for (int i_ = 0; i_ < 2; ++i_) *(LAS u32x4*)(L + AT_K + (st) * AT_KBYTES + (prow0 + 32 * i_) * AT_KSTR + pch * 16) = kreg[i_]; } while (0)
; #define AT_STOREV(st) do { _Pragma("unroll") for (int i_ = 0; i_ < 2; ++i_) *(LAS u32x4*)(L + AT_V + (st) * AT_VBYTES + (prow0 + 32 * i_) * AT_VSTR + pch * 16) = vreg[i_]; } while (0)
; __device__ __forceinline__ void attn_unit(const Frame& F, int layer, int qrow0, int ntiles, int b, int head, float lam, float m2, float lam_init) {
;     int tid_ = F.tid; asm volatile("" : "+v"(tid_));
;     const int tid = tid_, lane = tid & 63, wave = __builtin_amdgcn_readfirstlane(tid >> 6), r32 = lane & 31, hh = lane >> 5;
;     const int mp = wave & 1, qg = wave >> 1;
;     LAS unsigned char* L = F.lds;
;     const bf16_t* const Kp = F_K + head * 128; const bf16_t* const Vp = F_V + head * 128; bf16_t* const A2p = F_A2;
;     bf16x8 qf[4];
;     { const bf16_t* qp = F_Q + (size_t)(qrow0 + 32 * qg + r32) * 512 + head * 128 + mp * 64 + 8 * hh;
; #pragma unroll
;       for (int d0 = 0; d0 < 4; ++d0) qf[d0] = *(const bf16x8*)(qp + d0 * 16); }
;     f32x16 o[4];
; #pragma unroll
;     for (int j = 0; j < 4; ++j) o[j] = (f32x16){};
;     float lsum = 0.f;
;     f32x16 negm;
;     { float m2l = m2; asm volatile("" : "+v"(m2l));
; #pragma unroll
;       for (int t = 0; t < 16; ++t) negm[t] = -m2l; }
;     u32x4 kreg[2], vreg[2];
;     const int prow0 = tid >> 4, pch = tid & 15;
;     ...
;     if (wave >= 4) __builtin_amdgcn_s_setprio(1);
;     AT_LOADK(0); AT_LOADV(0); AT_STOREK(0); AT_STOREV(0);
;     if (ntiles > 1) { AT_LOADK(1); AT_STOREK(1); }
;     __syncthreads();
;     f32x16 sa, sb, na, nb;
;     AT_QK(sa, sb, 0);
;     lds_barrier();
.LBB0_549:
	s_add_u32 s42, s4, s30
	s_addc_u32 s43, s5, 0
	s_add_u32 s2, s2, s30
	s_addc_u32 s3, s3, 0
	s_lshl_b32 s4, s16, 8
	v_ashrrev_i32_e32 v186, 4, v32
	s_add_i32 s5, s4, 0x8000
	s_add_i32 s16, s4, 0x8040
	v_lshlrev_b32_e32 v3, 4, v32
	v_add_u32_e32 v128, s5, v186
	v_and_b32_e32 v144, 0xf0, v3
	v_add_u32_e32 v20, s16, v186
	v_lshl_add_u64 v[4:5], s[2:3], 0, v[144:145]
	s_mov_b64 s[2:3], 0x31534800
	v_ashrrev_i32_e32 v129, 31, v128
	v_ashrrev_i32_e32 v21, 31, v20
	v_lshl_add_u64 v[180:181], v[4:5], 0, s[2:3]
	v_lshlrev_b64 v[12:13], 10, v[128:129]
	s_mov_b64 s[2:3], 0x8000
	v_lshl_add_u64 v[16:17], s[42:43], 0, v[144:145]
	s_mov_b64 s[42:43], 0x33934800
	v_lshlrev_b64 v[62:63], 10, v[20:21]
	v_lshl_add_u64 v[14:15], v[12:13], 0, s[2:3]
	v_lshl_add_u64 v[182:183], v[16:17], 0, s[42:43]
	v_lshl_add_u64 v[96:97], v[62:63], 0, s[2:3]
	v_lshl_add_u64 v[4:5], v[180:181], 0, v[12:13]
	v_lshl_add_u64 v[8:9], v[180:181], 0, v[14:15]
	v_lshl_add_u64 v[12:13], v[182:183], 0, v[12:13]
	v_lshl_add_u64 v[16:17], v[182:183], 0, v[14:15]
	v_lshl_add_u64 v[20:21], v[180:181], 0, v[62:63]
	v_lshl_add_u64 v[24:25], v[180:181], 0, v[96:97]
	global_load_dwordx4 v[4:7], v[4:5], off
	s_nop 0
	global_load_dwordx4 v[8:11], v[8:9], off
	s_nop 0
	global_load_dwordx4 v[12:15], v[12:13], off
	s_nop 0
	global_load_dwordx4 v[16:19], v[16:17], off
	s_nop 0
	global_load_dwordx4 v[20:23], v[20:21], off
	s_nop 0
	global_load_dwordx4 v[24:27], v[24:25], off
	v_or_b32_e32 v1, s15, v1
	s_movk_i32 s16, 0x140
	v_mul_u32_u24_e32 v0, 0x110, v0
	v_mul_lo_u32 v198, v186, s24
	v_mul_lo_u32 v199, v186, s16
	v_lshlrev_b32_e32 v1, 1, v1
	v_add_u32_e32 v200, 0, v144
	v_xor_b32_e32 v64, 0x80000000, v2
	v_add_u32_e32 v2, 0x2800, v199
	v_add3_u32 v197, 0, v0, v1
	v_add_u32_e32 v144, v200, v198
	v_add_u32_e32 v194, v200, v199
	v_add_u32_e32 v195, v200, v2
	v_mov_b32_e32 v65, v64
	v_mov_b32_e32 v66, v64
	v_mov_b32_e32 v67, v64
	v_mov_b32_e32 v68, v64
	v_mov_b32_e32 v69, v64
	v_mov_b32_e32 v70, v64
	v_mov_b32_e32 v71, v64
	v_mov_b32_e32 v72, v64
	v_mov_b32_e32 v73, v64
	v_mov_b32_e32 v74, v64
	v_mov_b32_e32 v75, v64
	v_mov_b32_e32 v76, v64
	v_mov_b32_e32 v77, v64
	v_mov_b32_e32 v78, v64
	v_mov_b32_e32 v79, v64
	v_and_b32_e32 v193, 63, v32
	v_and_b32_e32 v33, 16, v32
	s_mov_b32 s15, 0x8000
	s_mov_b32 s2, 4
	s_mov_b32 s3, 0
	s_add_i32 s5, s4, 0x8080
	s_add_i32 s4, s4, 0x80c0
	s_waitcnt vmcnt(5)
	ds_write_b128 v144, v[4:7]
	s_waitcnt vmcnt(4)
	ds_write_b128 v144, v[8:11] offset:8704
	s_waitcnt vmcnt(3)
	ds_write_b128 v194, v[12:15] offset:34816
	s_waitcnt vmcnt(2)
	ds_write_b128 v195, v[16:19] offset:34816
	s_waitcnt vmcnt(1)
	ds_write_b128 v144, v[20:23] offset:17408
	s_waitcnt vmcnt(0)
	ds_write_b128 v144, v[24:27] offset:26112
	s_waitcnt lgkmcnt(0)
	s_barrier
	v_readfirstlane_b32 s72, v180
	v_readfirstlane_b32 s73, v181
	v_readfirstlane_b32 s74, v182
	v_readfirstlane_b32 s75, v183
	v_lshl_add_u32 v178, v186, 10, v200
	v_mov_b32_e32 v252, v64
	s_add_i32 s42, s4, 0xffffff40
	s_add_i32 s43, s4, 0xffff7f40
	s_lshl_b32 s43, s43, 3
	s_add_i32 s43, s43, 0xffffff00
	s_mov_b32 s2, 0
	s_add_i32 s5, s2, 2
	s_min_u32 s5, s5, 35
	s_cmp_lt_u32 s5, 4
	s_cselect_b32 s15, s42, s43
	s_lshl_b32 s45, s5, 6
	s_add_i32 s15, s15, s45
	s_lshl_b32 s15, s15, 10
	v_add_u32_e32 v186, s15, v178
	v_add_u32_e32 v187, 0x8000, v186
	global_load_dwordx4 v[162:165], v186, s[72:73]
	global_load_dwordx4 v[166:169], v187, s[72:73]
	s_add_i32 s5, s2, 1
	s_min_u32 s5, s5, 35
	s_cmp_lt_u32 s5, 4
	s_cselect_b32 s15, s42, s43
	s_lshl_b32 s45, s5, 6
	s_add_i32 s15, s15, s45
	s_lshl_b32 s15, s15, 10
	v_add_u32_e32 v188, s15, v178
	v_add_u32_e32 v189, 0x8000, v188
	global_load_dwordx4 v[170:173], v188, s[74:75]
	global_load_dwordx4 v[174:177], v189, s[74:75]
	v_bfe_u32 v186, v193, 2, 2
	v_lshrrev_b32_e32 v187, 5, v193
	v_lshl_add_u32 v186, v187, 2, v186
	v_mul_u32_u24_e32 v196, 0x140, v186
	v_bfe_u32 v187, v193, 4, 1
	v_and_b32_e32 v188, 3, v193
	v_lshl_add_u32 v196, v188, 3, v196
	v_lshl_add_u32 v196, v187, 5, v196
	v_mov_b32_e32 v0, 0
	v_mov_b32_e32 v1, 0
	v_mov_b32_e32 v2, 0
	v_mov_b32_e32 v3, 0
	v_mov_b32_e32 v4, 0
	v_mov_b32_e32 v5, 0
	v_mov_b32_e32 v6, 0
	v_mov_b32_e32 v7, 0
	v_mov_b32_e32 v8, 0
	v_mov_b32_e32 v9, 0
	v_mov_b32_e32 v10, 0
	v_mov_b32_e32 v11, 0
	v_mov_b32_e32 v12, 0
	v_mov_b32_e32 v13, 0
	v_mov_b32_e32 v14, 0
	v_mov_b32_e32 v15, 0
	v_mov_b32_e32 v16, 0
	v_mov_b32_e32 v17, 0
	v_mov_b32_e32 v18, 0
	v_mov_b32_e32 v19, 0
	v_mov_b32_e32 v20, 0
	v_mov_b32_e32 v21, 0
	v_mov_b32_e32 v22, 0
	v_mov_b32_e32 v23, 0
	v_mov_b32_e32 v24, 0
	v_mov_b32_e32 v25, 0
	v_mov_b32_e32 v26, 0
	v_mov_b32_e32 v27, 0
	v_mov_b32_e32 v28, 0
	v_mov_b32_e32 v29, 0
	v_mov_b32_e32 v30, 0
	v_mov_b32_e32 v31, 0
	v_mov_b32_e32 v32, 0
	v_mov_b32_e32 v33, 0
	v_mov_b32_e32 v34, 0
	v_mov_b32_e32 v35, 0
	v_mov_b32_e32 v36, 0
	v_mov_b32_e32 v37, 0
	v_mov_b32_e32 v38, 0
	v_mov_b32_e32 v39, 0
	v_mov_b32_e32 v40, 0
	v_mov_b32_e32 v41, 0
	v_mov_b32_e32 v42, 0
	v_mov_b32_e32 v43, 0
	v_mov_b32_e32 v44, 0
	v_mov_b32_e32 v45, 0
	v_mov_b32_e32 v46, 0
	v_mov_b32_e32 v47, 0
	v_mov_b32_e32 v48, 0
	v_mov_b32_e32 v49, 0
	v_mov_b32_e32 v50, 0
	v_mov_b32_e32 v51, 0
	v_mov_b32_e32 v52, 0
	v_mov_b32_e32 v53, 0
	v_mov_b32_e32 v54, 0
	v_mov_b32_e32 v55, 0
	v_mov_b32_e32 v56, 0
	v_mov_b32_e32 v57, 0
	v_mov_b32_e32 v58, 0
	v_mov_b32_e32 v59, 0
	v_mov_b32_e32 v60, 0
	v_mov_b32_e32 v61, 0
	v_mov_b32_e32 v62, 0
	v_mov_b32_e32 v63, 0
	v_mov_b32_e32 v201, 0
	v_mov_b32_e32 v180, 0
	v_mov_b32_e32 v181, 0
	v_mov_b32_e32 v182, 0
	v_mov_b32_e32 v183, 0
	v_mov_b32_e32 v218, 0
	v_mov_b32_e32 v219, 0
	v_mov_b32_e32 v220, 0
	v_mov_b32_e32 v221, 0
	v_mov_b32_e32 v222, 0
	v_mov_b32_e32 v223, 0
	v_mov_b32_e32 v224, 0
	v_mov_b32_e32 v225, 0
	v_mov_b32_e32 v226, 0
	v_mov_b32_e32 v227, 0
	v_mov_b32_e32 v228, 0
	v_mov_b32_e32 v229, 0
	v_mov_b32_e32 v230, 0
	v_mov_b32_e32 v231, 0
	v_mov_b32_e32 v232, 0
	v_mov_b32_e32 v233, 0
	ds_read_b128 v[128:131], v197 offset:0
	ds_read_b128 v[132:135], v197 offset:8704
	ds_read_b128 v[136:139], v197 offset:32
	ds_read_b128 v[140:143], v197 offset:8736
	s_waitcnt lgkmcnt(2)
	v_mfma_f32_32x32x16_bf16 v[80:95], v[128:131], v[158:161], v[64:79]
	v_mfma_f32_32x32x16_bf16 v[96:111], v[132:135], v[158:161], v[64:79]
	ds_read_b128 v[128:131], v197 offset:64
	ds_read_b128 v[132:135], v197 offset:8768
	s_waitcnt lgkmcnt(2)
	v_mfma_f32_32x32x16_bf16 v[80:95], v[136:139], v[154:157], v[80:95]
	v_mfma_f32_32x32x16_bf16 v[96:111], v[140:143], v[154:157], v[96:111]
	ds_read_b128 v[136:139], v197 offset:96
	ds_read_b128 v[140:143], v197 offset:8800
	s_waitcnt lgkmcnt(2)
	v_mfma_f32_32x32x16_bf16 v[80:95], v[128:131], v[150:153], v[80:95]
	v_mfma_f32_32x32x16_bf16 v[96:111], v[132:135], v[150:153], v[96:111]
	s_waitcnt lgkmcnt(0)
	v_mfma_f32_32x32x16_bf16 v[80:95], v[136:139], v[146:149], v[80:95]
	v_mfma_f32_32x32x16_bf16 v[96:111], v[140:143], v[146:149], v[96:111]
	s_cmp_lt_u32 s12, 4
	s_cbranch_scc1 .Latt_lead0
	s_barrier

; #define LAS __attribute__((address_space(3)))
; __device__ __forceinline__ unsigned pk2(float lo, float hi) { f32x2_t v = {lo, hi}; bf16x2_t b = __builtin_convertvector(v, bf16x2_t); return __builtin_bit_cast(unsigned, b); }
; __device__ __forceinline__ void attn_unit(const Frame& F, int layer, int qrow0, int ntiles, int b, int head, float lam, float m2, float lam_init) {
;     ...
;     for (int t = 0; t < ntiles; ++t) {
;         if (t + 2 < ntiles) AT_LOADK(t + 2);
;         if (t + 1 < ntiles) AT_LOADV(t + 1);
;         if (t + 1 < ntiles) AT_QK(na, nb, (t + 1) & 1);
;         float ls = 0.f;
; #pragma unroll
;         for (int i = 0; i < 16; ++i) { sa[i] = __builtin_amdgcn_exp2f(sa[i]); sb[i] = __builtin_amdgcn_exp2f(sb[i]); ls += sa[i] + sb[i]; }
;         lsum += ls;
;         bf16x8 pk[4];
;         { u32x4 w0, w1, w2, w3;
; #pragma unroll
;           for (int i = 0; i < 4; ++i) { w0[i] = pk2(sa[2 * i], sa[2 * i + 1]); w1[i] = pk2(sa[8 + 2 * i], sa[9 + 2 * i]); w2[i] = pk2(sb[2 * i], sb[2 * i + 1]); w3[i] = pk2(sb[8 + 2 * i], sb[9 + 2 * i]); }
;           pk[0] = __builtin_bit_cast(bf16x8, w0); pk[1] = __builtin_bit_cast(bf16x8, w1); pk[2] = __builtin_bit_cast(bf16x8, w2); pk[3] = __builtin_bit_cast(bf16x8, w3); }
;         LAS const unsigned char* Vt = L + AT_V + (t & 1) * AT_VBYTES;
;         __builtin_amdgcn_sched_barrier(0);
;         bf16x8 vfa[4], vfb[4];
; #pragma unroll
;         for (int j = 0; j < 4; ++j) vfa[j] = frag_tr_acc(Vt, AT_VSTR, 0, 32 * j, lane);
; #pragma unroll
;         for (int ks = 0; ks < 4; ks += 2) {
; #pragma unroll
;             for (int j = 0; j < 4; ++j) vfb[j] = frag_tr_acc(Vt, AT_VSTR, 16 * (ks + 1), 32 * j, lane);
; #pragma unroll
;             for (int j = 0; j < 4; ++j) o[j] = MFMA32(pk[ks], vfa[j], o[j]);
;             __builtin_amdgcn_sched_barrier(0);
;             if (ks + 2 < 4) {
; #pragma unroll
;                 for (int j = 0; j < 4; ++j) vfa[j] = frag_tr_acc(Vt, AT_VSTR, 16 * (ks + 2), 32 * j, lane);
;             }
; #pragma unroll
;             for (int j = 0; j < 4; ++j) o[j] = MFMA32(pk[ks + 1], vfb[j], o[j]);
;             __builtin_amdgcn_sched_barrier(0);
;         }
;         if (t + 2 < ntiles) AT_STOREK(t & 1);
;         if (t + 1 < ntiles) AT_STOREV((t + 1) & 1);
;         __syncthreads();
;         sa = na; sb = nb;
;     }
.Latt_loop:
	s_add_i32 s5, s2, 3
	s_min_u32 s5, s5, 35
	s_cmp_lt_u32 s5, 4
	s_cselect_b32 s15, s42, s43
	s_lshl_b32 s45, s5, 6
	s_add_i32 s15, s15, s45
	s_lshl_b32 s15, s15, 10
	v_add_u32_e32 v186, s15, v178
	v_add_u32_e32 v187, 0x8000, v186
	global_load_dwordx4 v[234:237], v186, s[72:73]
	global_load_dwordx4 v[238:241], v187, s[72:73]
	s_add_i32 s5, s2, 2
	s_min_u32 s5, s5, 35
	s_cmp_lt_u32 s5, 4
	s_cselect_b32 s15, s42, s43
	s_lshl_b32 s45, s5, 6
	s_add_i32 s15, s15, s45
	s_lshl_b32 s15, s15, 10
	v_add_u32_e32 v188, s15, v178
	v_add_u32_e32 v189, 0x8000, v188
	global_load_dwordx4 v[242:245], v188, s[74:75]
	global_load_dwordx4 v[248:251], v189, s[74:75]
	v_exp_f32_e32 v80, v80
	v_exp_f32_e32 v96, v96
	v_exp_f32_e32 v81, v81
	v_exp_f32_e32 v97, v97
	v_exp_f32_e32 v82, v82
	v_exp_f32_e32 v98, v98
	v_exp_f32_e32 v83, v83
	v_exp_f32_e32 v99, v99
	v_exp_f32_e32 v84, v84
	v_exp_f32_e32 v100, v100
	v_exp_f32_e32 v85, v85
	v_exp_f32_e32 v101, v101
	v_exp_f32_e32 v86, v86
	v_exp_f32_e32 v102, v102
	v_exp_f32_e32 v87, v87
	v_exp_f32_e32 v103, v103
	v_exp_f32_e32 v88, v88
	v_exp_f32_e32 v104, v104
	v_exp_f32_e32 v89, v89
	v_exp_f32_e32 v105, v105
	v_exp_f32_e32 v90, v90
	v_exp_f32_e32 v106, v106
	v_exp_f32_e32 v91, v91
	v_exp_f32_e32 v107, v107
	v_exp_f32_e32 v92, v92
	v_exp_f32_e32 v108, v108
	v_exp_f32_e32 v93, v93
	v_exp_f32_e32 v109, v109
	v_exp_f32_e32 v94, v94
	v_exp_f32_e32 v110, v110
	v_exp_f32_e32 v95, v95
	v_exp_f32_e32 v111, v111
	v_cvt_pk_bf16_f32 v112, v80, v81
	v_cvt_pk_bf16_f32 v113, v82, v83
	v_cvt_pk_bf16_f32 v114, v84, v85
	v_cvt_pk_bf16_f32 v115, v86, v87
	v_cvt_pk_bf16_f32 v116, v88, v89
	v_cvt_pk_bf16_f32 v117, v90, v91
	v_cvt_pk_bf16_f32 v118, v92, v93
	v_cvt_pk_bf16_f32 v119, v94, v95
	v_cvt_pk_bf16_f32 v120, v96, v97
	v_cvt_pk_bf16_f32 v121, v98, v99
	v_cvt_pk_bf16_f32 v122, v100, v101
	v_cvt_pk_bf16_f32 v123, v102, v103
	v_cvt_pk_bf16_f32 v124, v104, v105
	v_cvt_pk_bf16_f32 v125, v106, v107
	v_cvt_pk_bf16_f32 v126, v108, v109
	v_cvt_pk_bf16_f32 v127, v110, v111
	v_add_f32_e32 v80, v80, v96
	v_add_f32_e32 v81, v81, v97
	v_add_f32_e32 v82, v82, v98
	v_add_f32_e32 v83, v83, v99
	v_add_f32_e32 v84, v84, v100
	v_add_f32_e32 v85, v85, v101
	v_add_f32_e32 v86, v86, v102
	v_add_f32_e32 v87, v87, v103
	v_add_f32_e32 v88, v88, v104
	v_add_f32_e32 v89, v89, v105
	v_add_f32_e32 v90, v90, v106
	v_add_f32_e32 v91, v91, v107
	v_add_f32_e32 v92, v92, v108
	v_add_f32_e32 v93, v93, v109
	v_add_f32_e32 v94, v94, v110
	v_add_f32_e32 v95, v95, v111
	v_add_f32_e32 v80, v80, v88
	v_add_f32_e32 v81, v81, v89
	v_add_f32_e32 v82, v82, v90
	v_add_f32_e32 v83, v83, v91
	v_add_f32_e32 v84, v84, v92
	v_add_f32_e32 v85, v85, v93
	v_add_f32_e32 v86, v86, v94
	v_add_f32_e32 v87, v87, v95
	v_add_f32_e32 v80, v80, v84
	v_add_f32_e32 v81, v81, v85
	v_add_f32_e32 v82, v82, v86
	v_add_f32_e32 v83, v83, v87
	v_add_f32_e32 v80, v80, v82
	v_add_f32_e32 v81, v81, v83
	v_add_f32_e32 v80, v80, v81
	v_add_f32_e32 v201, v201, v80
	s_add_i32 s5, s2, 0
	s_and_b32 s5, s5, 1
	s_mul_i32 s15, s5, 0x5000
	v_add_u32_e32 v191, s15, v196
	s_mul_i32 s15, s5, 0x4400
	s_add_i32 s16, s2, 2
	s_cmp_ge_u32 s16, 36
	s_cselect_b32 s15, 80000, s15
	v_add_u32_e32 v179, s15, v144
	s_xor_b32 s5, s5, 1
	s_mul_i32 s15, s5, 0x4400
	v_add_u32_e32 v190, s15, v197
	s_mul_i32 s15, s5, 0x5000
	s_add_i32 s16, s2, 1
	s_cmp_ge_u32 s16, 36
	s_cselect_b32 s15, 62592, s15
	v_add_u32_e32 v185, s15, v194
	s_barrier
	s_waitcnt vmcnt(4)
	ds_write_b128 v179, v[162:165]
	ds_write_b128 v179, v[166:169] offset:8704
	ds_write_b128 v185, v[170:173] offset:34816
	ds_write_b128 v185, v[174:177] offset:45056
	ds_read_b128 v[128:131], v190 offset:0
	ds_read_b128 v[132:135], v190 offset:8704
	ds_read_b128 v[136:139], v190 offset:32
	ds_read_b128 v[140:143], v190 offset:8736
	ds_read_b64_tr_b16 v[202:203], v191 offset:34816
	ds_read_b64_tr_b16 v[206:207], v191 offset:34880
	ds_read_b64_tr_b16 v[210:211], v191 offset:34944
	ds_read_b64_tr_b16 v[214:215], v191 offset:35008
	s_waitcnt lgkmcnt(6)
	v_mfma_f32_32x32x16_bf16 v[80:95], v[128:131], v[158:161], v[64:79]
	v_mfma_f32_32x32x16_bf16 v[96:111], v[132:135], v[158:161], v[64:79]
	ds_read_b128 v[128:131], v190 offset:64
	ds_read_b128 v[132:135], v190 offset:8768
	ds_read_b64_tr_b16 v[204:205], v191 offset:37376
	ds_read_b64_tr_b16 v[208:209], v191 offset:37440
	ds_read_b64_tr_b16 v[212:213], v191 offset:37504
	ds_read_b64_tr_b16 v[216:217], v191 offset:37568
	s_waitcnt lgkmcnt(10)
	v_mfma_f32_32x32x16_bf16 v[80:95], v[136:139], v[154:157], v[80:95]
	v_mfma_f32_32x32x16_bf16 v[96:111], v[140:143], v[154:157], v[96:111]
	ds_read_b128 v[136:139], v190 offset:96
	ds_read_b128 v[140:143], v190 offset:8800
	s_waitcnt lgkmcnt(6)
	v_mfma_f32_32x32x16_bf16 v[80:95], v[128:131], v[150:153], v[80:95]
	v_mfma_f32_32x32x16_bf16 v[96:111], v[132:135], v[150:153], v[96:111]
	ds_read_b64_tr_b16 v[218:219], v191 offset:39936
	ds_read_b64_tr_b16 v[222:223], v191 offset:40000
	ds_read_b64_tr_b16 v[226:227], v191 offset:40064
	ds_read_b64_tr_b16 v[230:231], v191 offset:40128
	ds_read_b64_tr_b16 v[220:221], v191 offset:42496
	ds_read_b64_tr_b16 v[224:225], v191 offset:42560
	ds_read_b64_tr_b16 v[228:229], v191 offset:42624
	ds_read_b64_tr_b16 v[232:233], v191 offset:42688
	s_waitcnt lgkmcnt(8)
	v_mfma_f32_32x32x16_bf16 v[80:95], v[136:139], v[146:149], v[80:95]
	v_mfma_f32_32x32x16_bf16 v[96:111], v[140:143], v[146:149], v[96:111]
	v_mfma_f32_32x32x16_bf16 v[32:47], v[112:115], v[202:205], v[32:47]
	v_mfma_f32_32x32x16_bf16 v[48:63], v[112:115], v[206:209], v[48:63]
	v_mfma_f32_32x32x16_bf16 v[0:15], v[112:115], v[210:213], v[0:15]
	v_mfma_f32_32x32x16_bf16 v[16:31], v[112:115], v[214:217], v[16:31]
	ds_read_b64_tr_b16 v[202:203], v191 offset:45056
	ds_read_b64_tr_b16 v[206:207], v191 offset:45120
	ds_read_b64_tr_b16 v[210:211], v191 offset:45184
	ds_read_b64_tr_b16 v[214:215], v191 offset:45248
	ds_read_b64_tr_b16 v[204:205], v191 offset:47616
	ds_read_b64_tr_b16 v[208:209], v191 offset:47680
	ds_read_b64_tr_b16 v[212:213], v191 offset:47744
	s_waitcnt lgkmcnt(14)
; #define LAS __attribute__((address_space(3)))
; __device__ __forceinline__ unsigned pk2(float lo, float hi) { f32x2_t v = {lo, hi}; bf16x2_t b = __builtin_convertvector(v, bf16x2_t); return __builtin_bit_cast(unsigned, b); }
; __device__ __forceinline__ void attn_unit(const Frame& F, int layer, int qrow0, int ntiles, int b, int head, float lam, float m2, float lam_init) {
;     ...
;     for (int t = 0; t < ntiles; ++t) {
;         if (t + 2 < ntiles) AT_LOADK(t + 2);
;         if (t + 1 < ntiles) AT_LOADV(t + 1);
;         if (t + 1 < ntiles) AT_QK(na, nb, (t + 1) & 1);
;         float ls = 0.f;
; #pragma unroll
;         for (int i = 0; i < 16; ++i) { sa[i] = __builtin_amdgcn_exp2f(sa[i]); sb[i] = __builtin_amdgcn_exp2f(sb[i]); ls += sa[i] + sb[i]; }
;         lsum += ls;
;         bf16x8 pk[4];
;         { u32x4 w0, w1, w2, w3;
; #pragma unroll
;           for (int i = 0; i < 4; ++i) { w0[i] = pk2(sa[2 * i], sa[2 * i + 1]); w1[i] = pk2(sa[8 + 2 * i], sa[9 + 2 * i]); w2[i] = pk2(sb[2 * i], sb[2 * i + 1]); w3[i] = pk2(sb[8 + 2 * i], sb[9 + 2 * i]); }
;           pk[0] = __builtin_bit_cast(bf16x8, w0); pk[1] = __builtin_bit_cast(bf16x8, w1); pk[2] = __builtin_bit_cast(bf16x8, w2); pk[3] = __builtin_bit_cast(bf16x8, w3); }
;         LAS const unsigned char* Vt = L + AT_V + (t & 1) * AT_VBYTES;
;         __builtin_amdgcn_sched_barrier(0);
;         bf16x8 vfa[4], vfb[4];
; #pragma unroll
;         for (int j = 0; j < 4; ++j) vfa[j] = frag_tr_acc(Vt, AT_VSTR, 0, 32 * j, lane);
; #pragma unroll
;         for (int ks = 0; ks < 4; ks += 2) {
; #pragma unroll
;             for (int j = 0; j < 4; ++j) vfb[j] = frag_tr_acc(Vt, AT_VSTR, 16 * (ks + 1), 32 * j, lane);
; #pragma unroll
;             for (int j = 0; j < 4; ++j) o[j] = MFMA32(pk[ks], vfa[j], o[j]);
;             __builtin_amdgcn_sched_barrier(0);
;             if (ks + 2 < 4) {
; #pragma unroll
;                 for (int j = 0; j < 4; ++j) vfa[j] = frag_tr_acc(Vt, AT_VSTR, 16 * (ks + 2), 32 * j, lane);
;             }
; #pragma unroll
;             for (int j = 0; j < 4; ++j) o[j] = MFMA32(pk[ks + 1], vfb[j], o[j]);
;             __builtin_amdgcn_sched_barrier(0);
;         }
;         if (t + 2 < ntiles) AT_STOREK(t & 1);
;         if (t + 1 < ntiles) AT_STOREV((t + 1) & 1);
;         __syncthreads();
;         sa = na; sb = nb;
;     }
	ds_read_b64_tr_b16 v[216:217], v191 offset:47808
	s_waitcnt lgkmcnt(8)
	v_mfma_f32_32x32x16_bf16 v[32:47], v[116:119], v[218:221], v[32:47]
	v_mfma_f32_32x32x16_bf16 v[48:63], v[116:119], v[222:225], v[48:63]
	v_mfma_f32_32x32x16_bf16 v[0:15], v[116:119], v[226:229], v[0:15]
	v_mfma_f32_32x32x16_bf16 v[16:31], v[116:119], v[230:233], v[16:31]
	ds_read_b64_tr_b16 v[218:219], v191 offset:50176
	ds_read_b64_tr_b16 v[222:223], v191 offset:50240
	ds_read_b64_tr_b16 v[226:227], v191 offset:50304
	ds_read_b64_tr_b16 v[230:231], v191 offset:50368
	ds_read_b64_tr_b16 v[220:221], v191 offset:52736
	ds_read_b64_tr_b16 v[224:225], v191 offset:52800
	ds_read_b64_tr_b16 v[228:229], v191 offset:52864
	s_waitcnt lgkmcnt(14)
	ds_read_b64_tr_b16 v[232:233], v191 offset:52928
	s_waitcnt lgkmcnt(8)
	v_mfma_f32_32x32x16_bf16 v[32:47], v[120:123], v[202:205], v[32:47]
	v_mfma_f32_32x32x16_bf16 v[48:63], v[120:123], v[206:209], v[48:63]
	v_mfma_f32_32x32x16_bf16 v[0:15], v[120:123], v[210:213], v[0:15]
	v_mfma_f32_32x32x16_bf16 v[16:31], v[120:123], v[214:217], v[16:31]
	s_waitcnt lgkmcnt(0)
	v_mfma_f32_32x32x16_bf16 v[32:47], v[124:127], v[218:221], v[32:47]
	v_mfma_f32_32x32x16_bf16 v[48:63], v[124:127], v[222:225], v[48:63]
	v_mfma_f32_32x32x16_bf16 v[0:15], v[124:127], v[226:229], v[0:15]
	v_mfma_f32_32x32x16_bf16 v[16:31], v[124:127], v[230:233], v[16:31]
	s_barrier
	s_add_i32 s5, s2, 4
	s_min_u32 s5, s5, 35
	s_cmp_lt_u32 s5, 4
	s_cselect_b32 s15, s42, s43
	s_lshl_b32 s45, s5, 6
	s_add_i32 s15, s15, s45
	s_lshl_b32 s15, s15, 10
	v_add_u32_e32 v186, s15, v178
	v_add_u32_e32 v187, 0x8000, v186
	global_load_dwordx4 v[162:165], v186, s[72:73]
	global_load_dwordx4 v[166:169], v187, s[72:73]
	s_add_i32 s5, s2, 3
	s_min_u32 s5, s5, 35
	s_cmp_lt_u32 s5, 4
	s_cselect_b32 s15, s42, s43
	s_lshl_b32 s45, s5, 6
	s_add_i32 s15, s15, s45
	s_lshl_b32 s15, s15, 10
	v_add_u32_e32 v188, s15, v178
	v_add_u32_e32 v189, 0x8000, v188
	global_load_dwordx4 v[170:173], v188, s[74:75]
	global_load_dwordx4 v[174:177], v189, s[74:75]
	v_exp_f32_e32 v80, v80
	v_exp_f32_e32 v96, v96
	v_exp_f32_e32 v81, v81
	v_exp_f32_e32 v97, v97
	v_exp_f32_e32 v82, v82
	v_exp_f32_e32 v98, v98
	v_exp_f32_e32 v83, v83
	v_exp_f32_e32 v99, v99
	v_exp_f32_e32 v84, v84
	v_exp_f32_e32 v100, v100
	v_exp_f32_e32 v85, v85
	v_exp_f32_e32 v101, v101
	v_exp_f32_e32 v86, v86
	v_exp_f32_e32 v102, v102
	v_exp_f32_e32 v87, v87
	v_exp_f32_e32 v103, v103
	v_exp_f32_e32 v88, v88
	v_exp_f32_e32 v104, v104
	v_exp_f32_e32 v89, v89
	v_exp_f32_e32 v105, v105
	v_exp_f32_e32 v90, v90
	v_exp_f32_e32 v106, v106
	v_exp_f32_e32 v91, v91
	v_exp_f32_e32 v107, v107
	v_exp_f32_e32 v92, v92
	v_exp_f32_e32 v108, v108
	v_exp_f32_e32 v93, v93
	v_exp_f32_e32 v109, v109
	v_exp_f32_e32 v94, v94
	v_exp_f32_e32 v110, v110
	v_exp_f32_e32 v95, v95
	v_exp_f32_e32 v111, v111
	v_cvt_pk_bf16_f32 v112, v80, v81
	v_cvt_pk_bf16_f32 v113, v82, v83
	v_cvt_pk_bf16_f32 v114, v84, v85
	v_cvt_pk_bf16_f32 v115, v86, v87
	v_cvt_pk_bf16_f32 v116, v88, v89
	v_cvt_pk_bf16_f32 v117, v90, v91
	v_cvt_pk_bf16_f32 v118, v92, v93
	v_cvt_pk_bf16_f32 v119, v94, v95
	v_cvt_pk_bf16_f32 v120, v96, v97
	v_cvt_pk_bf16_f32 v121, v98, v99
	v_cvt_pk_bf16_f32 v122, v100, v101
	v_cvt_pk_bf16_f32 v123, v102, v103
	v_cvt_pk_bf16_f32 v124, v104, v105
	v_cvt_pk_bf16_f32 v125, v106, v107
	v_cvt_pk_bf16_f32 v126, v108, v109
	v_cvt_pk_bf16_f32 v127, v110, v111
	v_add_f32_e32 v80, v80, v96
	v_add_f32_e32 v81, v81, v97
	v_add_f32_e32 v82, v82, v98
	v_add_f32_e32 v83, v83, v99
	v_add_f32_e32 v84, v84, v100
	v_add_f32_e32 v85, v85, v101
	v_add_f32_e32 v86, v86, v102
	v_add_f32_e32 v87, v87, v103
	v_add_f32_e32 v88, v88, v104
	v_add_f32_e32 v89, v89, v105
	v_add_f32_e32 v90, v90, v106
	v_add_f32_e32 v91, v91, v107
	v_add_f32_e32 v92, v92, v108
	v_add_f32_e32 v93, v93, v109
	v_add_f32_e32 v94, v94, v110
	v_add_f32_e32 v95, v95, v111
	v_add_f32_e32 v80, v80, v88
	v_add_f32_e32 v81, v81, v89
	v_add_f32_e32 v82, v82, v90
	v_add_f32_e32 v83, v83, v91
	v_add_f32_e32 v84, v84, v92
	v_add_f32_e32 v85, v85, v93
	v_add_f32_e32 v86, v86, v94
	v_add_f32_e32 v87, v87, v95
	v_add_f32_e32 v80, v80, v84
	v_add_f32_e32 v81, v81, v85
	v_add_f32_e32 v82, v82, v86
	v_add_f32_e32 v83, v83, v87
	v_add_f32_e32 v80, v80, v82
	v_add_f32_e32 v81, v81, v83
	v_add_f32_e32 v80, v80, v81
	v_add_f32_e32 v201, v201, v80
	s_add_i32 s5, s2, 1
	s_and_b32 s5, s5, 1
	s_mul_i32 s15, s5, 0x5000
	v_add_u32_e32 v191, s15, v196
	s_mul_i32 s15, s5, 0x4400
	s_add_i32 s16, s2, 3
	s_cmp_ge_u32 s16, 36
	s_cselect_b32 s15, 80000, s15
	v_add_u32_e32 v179, s15, v144
	s_xor_b32 s5, s5, 1
	s_mul_i32 s15, s5, 0x4400
	v_add_u32_e32 v190, s15, v197
	s_mul_i32 s15, s5, 0x5000
	s_add_i32 s16, s2, 2
	s_cmp_ge_u32 s16, 36
	s_cselect_b32 s15, 62592, s15
	v_add_u32_e32 v185, s15, v194
	s_barrier
; #define LAS __attribute__((address_space(3)))
; __device__ __forceinline__ unsigned pk2(float lo, float hi) { f32x2_t v = {lo, hi}; bf16x2_t b = __builtin_convertvector(v, bf16x2_t); return __builtin_bit_cast(unsigned, b); }
; __device__ __forceinline__ void attn_unit(const Frame& F, int layer, int qrow0, int ntiles, int b, int head, float lam, float m2, float lam_init) {
;     ...
;     for (int t = 0; t < ntiles; ++t) {
;         if (t + 2 < ntiles) AT_LOADK(t + 2);
;         if (t + 1 < ntiles) AT_LOADV(t + 1);
;         if (t + 1 < ntiles) AT_QK(na, nb, (t + 1) & 1);
;         float ls = 0.f;
; #pragma unroll
;         for (int i = 0; i < 16; ++i) { sa[i] = __builtin_amdgcn_exp2f(sa[i]); sb[i] = __builtin_amdgcn_exp2f(sb[i]); ls += sa[i] + sb[i]; }
;         lsum += ls;
;         bf16x8 pk[4];
;         { u32x4 w0, w1, w2, w3;
; #pragma unroll
;           for (int i = 0; i < 4; ++i) { w0[i] = pk2(sa[2 * i], sa[2 * i + 1]); w1[i] = pk2(sa[8 + 2 * i], sa[9 + 2 * i]); w2[i] = pk2(sb[2 * i], sb[2 * i + 1]); w3[i] = pk2(sb[8 + 2 * i], sb[9 + 2 * i]); }
;           pk[0] = __builtin_bit_cast(bf16x8, w0); pk[1] = __builtin_bit_cast(bf16x8, w1); pk[2] = __builtin_bit_cast(bf16x8, w2); pk[3] = __builtin_bit_cast(bf16x8, w3); }
;         LAS const unsigned char* Vt = L + AT_V + (t & 1) * AT_VBYTES;
;         __builtin_amdgcn_sched_barrier(0);
;         bf16x8 vfa[4], vfb[4];
; #pragma unroll
;         for (int j = 0; j < 4; ++j) vfa[j] = frag_tr_acc(Vt, AT_VSTR, 0, 32 * j, lane);
; #pragma unroll
;         for (int ks = 0; ks < 4; ks += 2) {
; #pragma unroll
;             for (int j = 0; j < 4; ++j) vfb[j] = frag_tr_acc(Vt, AT_VSTR, 16 * (ks + 1), 32 * j, lane);
; #pragma unroll
;             for (int j = 0; j < 4; ++j) o[j] = MFMA32(pk[ks], vfa[j], o[j]);
;             __builtin_amdgcn_sched_barrier(0);
;             if (ks + 2 < 4) {
; #pragma unroll
;                 for (int j = 0; j < 4; ++j) vfa[j] = frag_tr_acc(Vt, AT_VSTR, 16 * (ks + 2), 32 * j, lane);
;             }
; #pragma unroll
;             for (int j = 0; j < 4; ++j) o[j] = MFMA32(pk[ks + 1], vfb[j], o[j]);
;             __builtin_amdgcn_sched_barrier(0);
;         }
;         if (t + 2 < ntiles) AT_STOREK(t & 1);
;         if (t + 1 < ntiles) AT_STOREV((t + 1) & 1);
;         __syncthreads();
;         sa = na; sb = nb;
;     }
	s_waitcnt vmcnt(4)
	ds_write_b128 v179, v[234:237]
	ds_write_b128 v179, v[238:241] offset:8704
	ds_write_b128 v185, v[242:245] offset:34816
	ds_write_b128 v185, v[248:251] offset:45056
	ds_read_b128 v[128:131], v190 offset:0
	ds_read_b128 v[132:135], v190 offset:8704
	ds_read_b128 v[136:139], v190 offset:32
	ds_read_b128 v[140:143], v190 offset:8736
	ds_read_b64_tr_b16 v[202:203], v191 offset:34816
	ds_read_b64_tr_b16 v[206:207], v191 offset:34880
	ds_read_b64_tr_b16 v[210:211], v191 offset:34944
	ds_read_b64_tr_b16 v[214:215], v191 offset:35008
	s_waitcnt lgkmcnt(6)
	v_mfma_f32_32x32x16_bf16 v[80:95], v[128:131], v[158:161], v[64:79]
	v_mfma_f32_32x32x16_bf16 v[96:111], v[132:135], v[158:161], v[64:79]
	ds_read_b128 v[128:131], v190 offset:64
	ds_read_b128 v[132:135], v190 offset:8768
	ds_read_b64_tr_b16 v[204:205], v191 offset:37376
	ds_read_b64_tr_b16 v[208:209], v191 offset:37440
	ds_read_b64_tr_b16 v[212:213], v191 offset:37504
	ds_read_b64_tr_b16 v[216:217], v191 offset:37568
	s_waitcnt lgkmcnt(10)
	v_mfma_f32_32x32x16_bf16 v[80:95], v[136:139], v[154:157], v[80:95]
	v_mfma_f32_32x32x16_bf16 v[96:111], v[140:143], v[154:157], v[96:111]
	ds_read_b128 v[136:139], v190 offset:96
	ds_read_b128 v[140:143], v190 offset:8800
	s_waitcnt lgkmcnt(6)
	v_mfma_f32_32x32x16_bf16 v[80:95], v[128:131], v[150:153], v[80:95]
	v_mfma_f32_32x32x16_bf16 v[96:111], v[132:135], v[150:153], v[96:111]
	ds_read_b64_tr_b16 v[218:219], v191 offset:39936
	ds_read_b64_tr_b16 v[222:223], v191 offset:40000
	ds_read_b64_tr_b16 v[226:227], v191 offset:40064
	ds_read_b64_tr_b16 v[230:231], v191 offset:40128
	ds_read_b64_tr_b16 v[220:221], v191 offset:42496
	ds_read_b64_tr_b16 v[224:225], v191 offset:42560
	ds_read_b64_tr_b16 v[228:229], v191 offset:42624
	ds_read_b64_tr_b16 v[232:233], v191 offset:42688
	s_waitcnt lgkmcnt(8)
	v_mfma_f32_32x32x16_bf16 v[80:95], v[136:139], v[146:149], v[80:95]
	v_mfma_f32_32x32x16_bf16 v[96:111], v[140:143], v[146:149], v[96:111]
	v_mfma_f32_32x32x16_bf16 v[32:47], v[112:115], v[202:205], v[32:47]
	v_mfma_f32_32x32x16_bf16 v[48:63], v[112:115], v[206:209], v[48:63]
	v_mfma_f32_32x32x16_bf16 v[0:15], v[112:115], v[210:213], v[0:15]
	v_mfma_f32_32x32x16_bf16 v[16:31], v[112:115], v[214:217], v[16:31]
	ds_read_b64_tr_b16 v[202:203], v191 offset:45056
	ds_read_b64_tr_b16 v[206:207], v191 offset:45120
	ds_read_b64_tr_b16 v[210:211], v191 offset:45184
	ds_read_b64_tr_b16 v[214:215], v191 offset:45248
	ds_read_b64_tr_b16 v[204:205], v191 offset:47616
	ds_read_b64_tr_b16 v[208:209], v191 offset:47680
	ds_read_b64_tr_b16 v[212:213], v191 offset:47744
	s_waitcnt lgkmcnt(14)
	ds_read_b64_tr_b16 v[216:217], v191 offset:47808
	s_waitcnt lgkmcnt(8)
	v_mfma_f32_32x32x16_bf16 v[32:47], v[116:119], v[218:221], v[32:47]
	v_mfma_f32_32x32x16_bf16 v[48:63], v[116:119], v[222:225], v[48:63]
	v_mfma_f32_32x32x16_bf16 v[0:15], v[116:119], v[226:229], v[0:15]
	v_mfma_f32_32x32x16_bf16 v[16:31], v[116:119], v[230:233], v[16:31]
	ds_read_b64_tr_b16 v[218:219], v191 offset:50176
	ds_read_b64_tr_b16 v[222:223], v191 offset:50240
	ds_read_b64_tr_b16 v[226:227], v191 offset:50304
	ds_read_b64_tr_b16 v[230:231], v191 offset:50368
	ds_read_b64_tr_b16 v[220:221], v191 offset:52736
	ds_read_b64_tr_b16 v[224:225], v191 offset:52800
	ds_read_b64_tr_b16 v[228:229], v191 offset:52864
	s_waitcnt lgkmcnt(14)
	ds_read_b64_tr_b16 v[232:233], v191 offset:52928
	s_waitcnt lgkmcnt(8)
	v_mfma_f32_32x32x16_bf16 v[32:47], v[120:123], v[202:205], v[32:47]
	v_mfma_f32_32x32x16_bf16 v[48:63], v[120:123], v[206:209], v[48:63]
	v_mfma_f32_32x32x16_bf16 v[0:15], v[120:123], v[210:213], v[0:15]
	v_mfma_f32_32x32x16_bf16 v[16:31], v[120:123], v[214:217], v[16:31]
	s_waitcnt lgkmcnt(0)
	v_mfma_f32_32x32x16_bf16 v[32:47], v[124:127], v[218:221], v[32:47]
	v_mfma_f32_32x32x16_bf16 v[48:63], v[124:127], v[222:225], v[48:63]
	v_mfma_f32_32x32x16_bf16 v[0:15], v[124:127], v[226:229], v[0:15]
	v_mfma_f32_32x32x16_bf16 v[16:31], v[124:127], v[230:233], v[16:31]
	s_barrier
	s_add_i32 s2, s2, 2
	s_cmp_lt_u32 s2, 36
	s_cbranch_scc1 .Latt_loop
	s_waitcnt vmcnt(0)
	s_cmp_ge_u32 s12, 4
	s_cbranch_scc1 .Latt_trail1
	s_barrier
